# P6 reuses the expert tables left in LDS by the gate_up phase (no count reload), first queue ticket of each MoE phase claimed at the phase start
# baseline (speedup 1.0000x reference)
; #define LAS3 __attribute__((address_space(3)))
; __device__ __forceinline__ int lane_id() { int r; asm volatile("v_mbcnt_lo_u32_b32 %0, -1, 0\n\tv_mbcnt_hi_u32_b32 %0, -1, %0" : "=v"(r)); return r; }
; #define LD_WAIT(r) asm volatile("s_waitcnt vmcnt(0)" : "+v"(r) :: "memory")
; __device__ __forceinline__ unsigned xb_xcc_id() { return (unsigned)__builtin_amdgcn_s_getreg((3 << 11) | 20) & 0xFu; }
; template <int EPI>
; __device__ __forceinline__ int* moe_phase(const Params& p, LAS3 char* lds, int wid, int* pend_in) {
;     ...
;     __syncthreads();
;     LAS3 int* xcnt = (LAS3 int*)(lds + LDS_MISC + 1024);
;     { const int t0 = wid * 64 + lane_id(); if (t0 < NE) { const int c = p.cnt[t0]; mtv[t0] = (c + 255) >> 8; xcnt[t0] = c; } }
;     __syncthreads();
;     ...
;     const int q0 = (int)(xb_xcc_id() & 7u);
;     GemmArgs g{};
;     if (EPI == 2) { g.A = p.xn2; g.B = p.w_gate_up; g.C = p.act; g.bias = p.b_gate_up; g.list = p.list; }
;     else { g.A = p.act; g.B = p.w_down; g.C = p.outp; g.bias = p.b_down; }
;     __syncthreads();
;     { const int t0 = wid * 64 + lane_id(); if (t0 == 0) { unsigned c0 = inc_early(&qctr[q0]); LD_WAIT(c0); slot[0] = ((unsigned)q0 << 20) | c0; } }
.LBB0_406:
	s_or_b64 exec, exec, s[0:1]
	s_waitcnt lgkmcnt(0)
	s_barrier
	s_barrier
	v_mbcnt_lo_u32_b32 v20, -1, 0
	v_mbcnt_hi_u32_b32 v20, -1, v20
	s_nop 0
	v_sub_u32_e32 v20, 0, v20
	v_cmp_eq_u32_e32 vcc, s75, v20
	s_and_saveexec_b64 s[0:1], vcc
	s_cbranch_execz .Ltk1_p5
	v_readlane_b32 s100, v254, 32
	v_readlane_b32 s101, v254, 33
	s_getreg_b32 vcc_lo, hwreg(HW_REG_XCC_ID, 0, 4)
	s_and_b32 vcc_lo, vcc_lo, 7
	s_lshl_b32 vcc_lo, vcc_lo, 2
	s_add_u32 s100, s100, vcc_lo
	s_addc_u32 s101, s101, 0
	v_mov_b32_e32 v20, 0
	v_mov_b32_e32 v21, 1
	s_nop 4
	global_atomic_add v21, v20, v21, s[100:101] sc0
.Ltk1_p5:
	s_or_b64 exec, exec, s[0:1]
	v_mbcnt_lo_u32_b32 v0, -1, 0
	v_mbcnt_hi_u32_b32 v0, -1, v0
	s_nop 0
	v_add_u32_e32 v0, s75, v0
	v_cmp_gt_i32_e32 vcc, 32, v0
	s_and_saveexec_b64 s[0:1], vcc
	s_cbranch_execz .LBB0_408
	v_readlane_b32 s4, v254, 2
	v_ashrrev_i32_e32 v1, 31, v0
	v_readlane_b32 s14, v254, 12
	v_readlane_b32 s15, v254, 13
	v_readlane_b32 s5, v254, 3
	v_readlane_b32 s6, v254, 4
	v_lshl_add_u64 v[2:3], v[0:1], 2, s[14:15]
	global_load_dword v1, v[2:3], off
	v_lshl_add_u32 v0, v0, 2, 0
	v_add_u32_e32 v2, 0x21300, v0
	v_readlane_b32 s7, v254, 5
	v_readlane_b32 s8, v254, 6
	v_readlane_b32 s9, v254, 7
	v_readlane_b32 s10, v254, 8
	v_readlane_b32 s11, v254, 9
	v_readlane_b32 s12, v254, 10
	v_readlane_b32 s13, v254, 11
	v_readlane_b32 s16, v254, 14
	v_readlane_b32 s17, v254, 15
	v_readlane_b32 s18, v254, 16
	v_readlane_b32 s19, v254, 17
	v_add_u32_e32 v0, 0x21400, v0
	s_waitcnt vmcnt(0)
	v_add_u32_e32 v3, 0xff, v1
	v_ashrrev_i32_e32 v3, 8, v3
	ds_write_b32 v2, v3
	ds_write_b32 v0, v1

; __device__ __forceinline__ int lane_id() { int r; asm volatile("v_mbcnt_lo_u32_b32 %0, -1, 0\n\tv_mbcnt_hi_u32_b32 %0, -1, %0" : "=v"(r)); return r; }
; #define LD_WAIT(r) asm volatile("s_waitcnt vmcnt(0)" : "+v"(r) :: "memory")
; __device__ __forceinline__ unsigned xb_xcc_id() { return (unsigned)__builtin_amdgcn_s_getreg((3 << 11) | 20) & 0xFu; }
; template <int EPI>
; __device__ __forceinline__ int* moe_phase(const Params& p, LAS3 char* lds, int wid, int* pend_in) {
;     ...
;     __syncthreads();
;     const int q0 = (int)(xb_xcc_id() & 7u);
;     GemmArgs g{};
;     if (EPI == 2) { g.A = p.xn2; g.B = p.w_gate_up; g.C = p.act; g.bias = p.b_gate_up; g.list = p.list; }
;     else { g.A = p.act; g.B = p.w_down; g.C = p.outp; g.bias = p.b_down; }
;     __syncthreads();
;     { const int t0 = wid * 64 + lane_id(); if (t0 == 0) { unsigned c0 = inc_early(&qctr[q0]); LD_WAIT(c0); slot[0] = ((unsigned)q0 << 20) | c0; } }
.LBB0_428:
	s_or_b64 exec, exec, s[0:1]
	s_waitcnt lgkmcnt(0)
	s_barrier
	s_getreg_b32 s2, hwreg(HW_REG_XCC_ID, 0, 4)
	s_barrier
	v_mbcnt_lo_u32_b32 v0, -1, 0
	v_mbcnt_hi_u32_b32 v0, -1, v0
	s_mov_b32 s5, 0
	v_sub_u32_e32 v0, 0, v0
	v_cmp_eq_u32_e32 vcc, s75, v0
	s_and_saveexec_b64 s[0:1], vcc
	s_cbranch_execz .LBB0_430
	s_and_b32 s4, s2, 7
	v_readlane_b32 s8, v254, 20
	s_lshl_b32 s2, s4, 2
	v_readlane_b32 s20, v254, 32
	v_readlane_b32 s21, v254, 33
	s_add_u32 s2, s20, s2
	s_addc_u32 s3, s21, 0
	s_add_i32 s2, 0, 0x21040
	s_waitcnt vmcnt(0)
	v_readlane_b32 s9, v254, 21
	v_lshl_or_b32 v0, s4, 20, v21
	v_mov_b32_e32 v1, s2
	v_readlane_b32 s10, v254, 22
	v_readlane_b32 s11, v254, 23
	v_readlane_b32 s12, v254, 24
	v_readlane_b32 s13, v254, 25
	v_readlane_b32 s14, v254, 26
	v_readlane_b32 s15, v254, 27
	v_readlane_b32 s16, v254, 28
	v_readlane_b32 s17, v254, 29
	v_readlane_b32 s18, v254, 30
	v_readlane_b32 s19, v254, 31
	v_readlane_b32 s22, v254, 34
	v_readlane_b32 s23, v254, 35
	ds_write_b32 v1, v0

; #define LAS3 __attribute__((address_space(3)))
; __device__ __forceinline__ int lane_id() { int r; asm volatile("v_mbcnt_lo_u32_b32 %0, -1, 0\n\tv_mbcnt_hi_u32_b32 %0, -1, %0" : "=v"(r)); return r; }
; #define LD_WAIT(r) asm volatile("s_waitcnt vmcnt(0)" : "+v"(r) :: "memory")
; __device__ __forceinline__ unsigned xb_xcc_id() { return (unsigned)__builtin_amdgcn_s_getreg((3 << 11) | 20) & 0xFu; }
; template <int EPI>
; __device__ __forceinline__ int* moe_phase(const Params& p, LAS3 char* lds, int wid, int* pend_in) {
;     ...
;     __syncthreads();
;     LAS3 int* xcnt = (LAS3 int*)(lds + LDS_MISC + 1024);
;     { const int t0 = wid * 64 + lane_id(); if (t0 < NE) { const int c = p.cnt[t0]; mtv[t0] = (c + 255) >> 8; xcnt[t0] = c; } }
;     __syncthreads();
;     ...
;     const int q0 = (int)(xb_xcc_id() & 7u);
;     GemmArgs g{};
;     if (EPI == 2) { g.A = p.xn2; g.B = p.w_gate_up; g.C = p.act; g.bias = p.b_gate_up; g.list = p.list; }
;     else { g.A = p.act; g.B = p.w_down; g.C = p.outp; g.bias = p.b_down; }
;     __syncthreads();
;     { const int t0 = wid * 64 + lane_id(); if (t0 == 0) { unsigned c0 = inc_early(&qctr[q0]); LD_WAIT(c0); slot[0] = ((unsigned)q0 << 20) | c0; } }
.LBB0_510:
	s_or_b64 exec, exec, s[0:1]
	s_waitcnt lgkmcnt(0)
	s_barrier
	v_mbcnt_lo_u32_b32 v20, -1, 0
	v_mbcnt_hi_u32_b32 v20, -1, v20
	s_nop 0
	v_sub_u32_e32 v20, 0, v20
	v_cmp_eq_u32_e32 vcc, s75, v20
	s_and_saveexec_b64 s[0:1], vcc
	s_cbranch_execz .Ltk1_p6
	v_readlane_b32 s100, v254, 32
	v_readlane_b32 s101, v254, 33
	s_getreg_b32 vcc_lo, hwreg(HW_REG_XCC_ID, 0, 4)
	s_and_b32 vcc_lo, vcc_lo, 7
	s_lshl_b32 vcc_lo, vcc_lo, 2
	s_add_u32 s100, s100, vcc_lo
	s_addc_u32 s101, s101, 0
	v_mov_b32_e32 v20, 0
	v_mov_b32_e32 v21, 1
	s_nop 4
	global_atomic_add v21, v20, v21, s[100:101] offset:32 sc0
.Ltk1_p6:
	s_or_b64 exec, exec, s[0:1]
	v_mbcnt_lo_u32_b32 v0, -1, 0
	v_mbcnt_hi_u32_b32 v0, -1, v0
	s_nop 0
	v_add_u32_e32 v0, s75, v0
	v_cmp_gt_i32_e32 vcc, 32, v0
	s_and_saveexec_b64 s[0:1], vcc
	s_branch .LBB0_512
	v_readlane_b32 s8, v254, 2
	v_ashrrev_i32_e32 v1, 31, v0
	v_readlane_b32 s18, v254, 12
	v_readlane_b32 s19, v254, 13
	v_readlane_b32 s9, v254, 3
	v_readlane_b32 s10, v254, 4
	v_lshl_add_u64 v[2:3], v[0:1], 2, s[18:19]
	global_load_dword v1, v[2:3], off
	v_lshl_add_u32 v0, v0, 2, 0
	v_add_u32_e32 v2, 0x21300, v0
	v_readlane_b32 s11, v254, 5
	v_readlane_b32 s12, v254, 6
	v_readlane_b32 s13, v254, 7
	v_readlane_b32 s14, v254, 8
	v_readlane_b32 s15, v254, 9
	v_readlane_b32 s16, v254, 10
	v_readlane_b32 s17, v254, 11
	v_readlane_b32 s20, v254, 14
	v_readlane_b32 s21, v254, 15
	v_readlane_b32 s22, v254, 16
	v_readlane_b32 s23, v254, 17
	v_add_u32_e32 v0, 0x21400, v0
	s_waitcnt vmcnt(0)
	v_add_u32_e32 v3, 0xff, v1
	v_ashrrev_i32_e32 v3, 8, v3
	ds_write_b32 v2, v3
	ds_write_b32 v0, v1

; __device__ __forceinline__ int lane_id() { int r; asm volatile("v_mbcnt_lo_u32_b32 %0, -1, 0\n\tv_mbcnt_hi_u32_b32 %0, -1, %0" : "=v"(r)); return r; }
; #define LD_WAIT(r) asm volatile("s_waitcnt vmcnt(0)" : "+v"(r) :: "memory")
; __device__ __forceinline__ unsigned xb_xcc_id() { return (unsigned)__builtin_amdgcn_s_getreg((3 << 11) | 20) & 0xFu; }
; template <int EPI>
; __device__ __forceinline__ int* moe_phase(const Params& p, LAS3 char* lds, int wid, int* pend_in) {
;     ...
;     __syncthreads();
;     const int q0 = (int)(xb_xcc_id() & 7u);
;     GemmArgs g{};
;     if (EPI == 2) { g.A = p.xn2; g.B = p.w_gate_up; g.C = p.act; g.bias = p.b_gate_up; g.list = p.list; }
;     else { g.A = p.act; g.B = p.w_down; g.C = p.outp; g.bias = p.b_down; }
;     __syncthreads();
;     { const int t0 = wid * 64 + lane_id(); if (t0 == 0) { unsigned c0 = inc_early(&qctr[q0]); LD_WAIT(c0); slot[0] = ((unsigned)q0 << 20) | c0; } }
.LBB0_516:
	s_or_b64 exec, exec, s[0:1]
	v_readlane_b32 s8, v254, 20
	v_readlane_b32 s9, v254, 21
	v_readlane_b32 s10, v254, 22
	v_readlane_b32 s11, v254, 23
	v_readlane_b32 s12, v254, 24
	v_readlane_b32 s13, v254, 25
	v_readlane_b32 s14, v254, 26
	v_readlane_b32 s15, v254, 27
	v_readlane_b32 s16, v254, 28
	v_readlane_b32 s17, v254, 29
	v_readlane_b32 s18, v254, 30
	v_readlane_b32 s19, v254, 31
	v_readlane_b32 s20, v254, 32
	v_readlane_b32 s21, v254, 33
	v_readlane_b32 s22, v254, 34
	v_readlane_b32 s23, v254, 35
	s_mov_b64 s[8:9], s[16:17]
	s_mov_b64 s[12:13], s[20:21]
	s_waitcnt lgkmcnt(0)
	s_barrier
	s_getreg_b32 s4, hwreg(HW_REG_XCC_ID, 0, 4)
	s_barrier
	v_mbcnt_lo_u32_b32 v0, -1, 0
	v_mbcnt_hi_u32_b32 v0, -1, v0
	s_add_u32 s2, s12, 32
	v_sub_u32_e32 v0, 0, v0
	s_addc_u32 s3, s13, 0
	s_mov_b32 s5, 0
	v_cmp_eq_u32_e32 vcc, s75, v0
	s_mov_b64 s[10:11], s[18:19]
	s_mov_b64 s[14:15], s[22:23]
	s_and_saveexec_b64 s[0:1], vcc
	s_cbranch_execz .LBB0_518
	s_and_b32 s4, s4, 7
	s_lshl_b32 s7, s4, 2
	s_add_u32 s8, s2, s7
	s_addc_u32 s9, s3, 0
	s_add_i32 s7, 0, 0x21040
	s_waitcnt vmcnt(0)
	s_nop 0
	v_lshl_or_b32 v0, s4, 20, v21
	v_mov_b32_e32 v1, s7
	ds_write_b32 v1, v0
